# GQA loop: fewer exps ahead of the first QK MFMA
# baseline (speedup 1.0000x reference)
; #define LAS __attribute__((address_space(3)))
; #define ATT_PKN(P, BASE, OUT) do { u32x4 w = {cvt_pk_bf16(P[BASE + 0], P[BASE + 1]), cvt_pk_bf16(P[BASE + 2], P[BASE + 3]), cvt_pk_bf16(P[BASE + 4], P[BASE + 5]), cvt_pk_bf16(P[BASE + 6], P[BASE + 7])}; \
;     OUT = __builtin_bit_cast(bf16x8, w); } while (0)
; __device__ __forceinline__ void finishSM(f32x16& p0, f32x16& p1, float alpha, float& l_reg, bf16x8& pa0, bf16x8& pa1, bf16x8& pa2, bf16x8& pa3) {
; #pragma unroll
;     for (int r = 0; r < 16; ++r) p1[r] = EXP_PROBE ? fmaf(p1[r], 0.001f, 1.f) : __builtin_amdgcn_exp2f(p1[r]);
;     float ps = 0.f;
; #pragma unroll
;     for (int r = 0; r < 16; ++r) ps += p0[r];
; #pragma unroll
;     for (int r = 0; r < 16; ++r) ps += p1[r];
;     { auto rr = __builtin_amdgcn_permlane32_swap(__float_as_uint(ps), __float_as_uint(ps), false, false);
;       ps = __uint_as_float(rr[0]) + __uint_as_float(rr[1]); }
;     l_reg = l_reg * alpha + ps;
;     ATT_PKN(p0, 0, pa0); ATT_PKN(p0, 8, pa1); ATT_PKN(p1, 0, pa2); ATT_PKN(p1, 8, pa3);
; }
; template <int DQK> __device__ __forceinline__ void qkt(f32x16& p0, f32x16& p1, const LAS char* buf, const bf16x8* qr, int r32, int hi, const f32x16& negm) {
; #pragma unroll
;     for (int d0 = 0; d0 < 4; ++d0) { const int ch = d0 * 2 + hi;
;         const bf16x8 b0 = *(const LAS bf16x8*)(buf + B_KN + swz64(r32, ch));
;         const bf16x8 b1 = *(const LAS bf16x8*)(buf + B_KN + swz64(32 + r32, ch));
;         p0 = __builtin_amdgcn_mfma_f32_32x32x16_bf16(b0, qr[d0], d0 == 0 ? negm : p0, 0, 0, 0);
;         p1 = __builtin_amdgcn_mfma_f32_32x32x16_bf16(b1, qr[d0], d0 == 0 ? negm : p1, 0, 0, 0); }
;     if constexpr (DQK == 96) {
; #pragma unroll
;         for (int d0 = 0; d0 < 2; ++d0) { const int ch = d0 * 2 + hi;
;             const bf16x8 b0 = *(const LAS bf16x8*)(buf + B_KR + swz32(r32, ch));
;             const bf16x8 b1 = *(const LAS bf16x8*)(buf + B_KR + swz32(32 + r32, ch));
;             p0 = __builtin_amdgcn_mfma_f32_32x32x16_bf16(b0, qr[4 + d0], p0, 0, 0, 0);
;             p1 = __builtin_amdgcn_mfma_f32_32x32x16_bf16(b1, qr[4 + d0], p1, 0, 0, 0); }
;     }
.LBB0_497:
	s_mov_b32 s1, s11
	s_mov_b32 s11, s35
	s_waitcnt lgkmcnt(0)
	s_barrier
	v_add_u32_e32 v252, s1, v208
	v_add_u32_e32 v228, v252, v209
	ds_read_b128 v[224:227], v228
	ds_read_b128 v[228:231], v228 offset:4096
	v_add_u32_e32 v236, v252, v210
	ds_read_b128 v[232:235], v236
	ds_read_b128 v[236:239], v236 offset:4096
	v_add_u32_e32 v244, v252, v211
	ds_read_b128 v[240:243], v244
	ds_read_b128 v[244:247], v244 offset:4096
	v_add_u32_e32 v253, v252, v212
	ds_read_b128 v[248:251], v253
	v_exp_f32_e32 v66, v66
	v_exp_f32_e32 v67, v67
	v_exp_f32_e32 v68, v68
	v_exp_f32_e32 v69, v69
	s_waitcnt lgkmcnt(6)
	v_mfma_f32_32x32x16_bf16 v[98:113], v[224:227], v[114:117], v[18:33]
	ds_read_b128 v[224:227], v253 offset:4096
	v_exp_f32_e32 v70, v70
	v_exp_f32_e32 v71, v71
	v_exp_f32_e32 v72, v72
	v_exp_f32_e32 v73, v73
	v_cvt_pk_bf16_f32 v156, v143, v145
	v_cvt_pk_bf16_f32 v157, v141, v144
	v_add_f32_e32 v164, 0, v143
	v_add_f32_e32 v164, v145, v164
	s_waitcnt lgkmcnt(6)
	v_mfma_f32_32x32x16_bf16 v[82:97], v[228:231], v[114:117], v[18:33]
	v_exp_f32_e32 v74, v74
	v_exp_f32_e32 v75, v75
	v_exp_f32_e32 v76, v76
	v_exp_f32_e32 v77, v77
	v_cvt_pk_bf16_f32 v158, v139, v142
	v_cvt_pk_bf16_f32 v159, v138, v140
	v_add_f32_e32 v164, v141, v164
	v_add_f32_e32 v164, v144, v164
	s_waitcnt lgkmcnt(5)
	v_mfma_f32_32x32x16_bf16 v[98:113], v[232:235], v[12:15], v[98:113]
	v_exp_f32_e32 v78, v78
	v_exp_f32_e32 v79, v79
	v_exp_f32_e32 v80, v80
	v_exp_f32_e32 v81, v81
	v_cvt_pk_bf16_f32 v160, v151, v153
	v_cvt_pk_bf16_f32 v161, v149, v152
	v_add_f32_e32 v164, v139, v164
	v_add_f32_e32 v164, v142, v164
	s_waitcnt lgkmcnt(4)
	v_mfma_f32_32x32x16_bf16 v[82:97], v[236:239], v[12:15], v[82:97]
	v_cvt_pk_bf16_f32 v162, v147, v150
	v_cvt_pk_bf16_f32 v163, v146, v148
	v_add_f32_e32 v164, v138, v164
	v_add_f32_e32 v164, v140, v164
	v_add_f32_e32 v164, v151, v164
	v_add_f32_e32 v164, v153, v164
	v_add_f32_e32 v164, v149, v164
	v_add_f32_e32 v164, v152, v164
	v_add_f32_e32 v164, v147, v164
	v_add_f32_e32 v164, v150, v164
	v_add_f32_e32 v164, v146, v164
	v_add_f32_e32 v164, v148, v164
	s_waitcnt lgkmcnt(3)
	v_mfma_f32_32x32x16_bf16 v[98:113], v[240:243], v[8:11], v[98:113]
	v_add_u32_e32 v2, s11, v213
	ds_read_b64_tr_b16 v[138:139], v2 offset:0
	ds_read_b64_tr_b16 v[140:141], v2 offset:1024
	ds_read_b64_tr_b16 v[142:143], v2 offset:2048
	ds_read_b64_tr_b16 v[144:145], v2 offset:3072
	v_add_f32_e32 v164, v66, v164
	v_add_f32_e32 v164, v67, v164
	v_add_f32_e32 v164, v68, v164
	v_add_f32_e32 v164, v69, v164
	s_waitcnt lgkmcnt(6)
	v_mfma_f32_32x32x16_bf16 v[82:97], v[244:247], v[8:11], v[82:97]
	ds_read_b64_tr_b16 v[146:147], v2 offset:4096
	ds_read_b64_tr_b16 v[148:149], v2 offset:5120
	ds_read_b64_tr_b16 v[150:151], v2 offset:6144
	ds_read_b64_tr_b16 v[152:153], v2 offset:7168
	v_add_f32_e32 v164, v70, v164
	v_add_f32_e32 v164, v71, v164
	v_add_f32_e32 v164, v72, v164
	v_add_f32_e32 v164, v73, v164
	s_waitcnt lgkmcnt(9)
	v_mfma_f32_32x32x16_bf16 v[98:113], v[248:251], v[4:7], v[98:113]
	v_add_f32_e32 v164, v74, v164
	v_add_f32_e32 v164, v75, v164
	v_add_f32_e32 v164, v76, v164
	v_add_f32_e32 v164, v77, v164
	s_waitcnt lgkmcnt(8)
	v_mfma_f32_32x32x16_bf16 v[82:97], v[224:227], v[4:7], v[82:97]
	ds_read_b64_tr_b16 v[224:225], v2 offset:512
	ds_read_b64_tr_b16 v[226:227], v2 offset:1536
	ds_read_b64_tr_b16 v[228:229], v2 offset:2560
	ds_read_b64_tr_b16 v[230:231], v2 offset:3584
	ds_read_b64_tr_b16 v[232:233], v2 offset:4608
	ds_read_b64_tr_b16 v[234:235], v2 offset:5632
	ds_read_b64_tr_b16 v[236:237], v2 offset:6656
	ds_read_b64_tr_b16 v[238:239], v2 offset:7680
	s_waitcnt lgkmcnt(8)
	v_mfma_f32_32x32x16_bf16 v[50:65], v[138:141], v[156:159], v[50:65]
	v_add_f32_e32 v164, v78, v164
	v_add_f32_e32 v164, v79, v164
	v_add_f32_e32 v164, v80, v164
	v_add_f32_e32 v154, v81, v164
	v_mov_b32_e32 v155, v154
	v_mfma_f32_32x32x16_bf16 v[50:65], v[142:145], v[160:163], v[50:65]
	v_cvt_pk_bf16_f32 v66, v66, v67
	v_cvt_pk_bf16_f32 v67, v68, v69
	v_cvt_pk_bf16_f32 v68, v70, v71
	v_cvt_pk_bf16_f32 v69, v72, v73
	v_cvt_pk_bf16_f32 v70, v74, v75
	v_cvt_pk_bf16_f32 v71, v76, v77
	v_cvt_pk_bf16_f32 v72, v78, v79
	v_cvt_pk_bf16_f32 v73, v80, v81
	v_permlane32_swap_b32_e32 v154, v155
	v_mfma_f32_32x32x16_bf16 v[50:65], v[146:149], v[66:69], v[50:65]
	s_add_i32 s8, s13, -1
	s_cmp_lt_u32 s8, s31
	s_cselect_b32 s9, 0, s31
	s_cselect_b32 s35, s12, s29
	s_lshl_b32 s9, s9, 6
	s_sub_i32 s9, s35, s9
	v_add_u32_e32 v252, s9, v137
	v_subrev_u32_e32 v126, 64, v252
	v_ashrrev_i32_e32 v127, 31, v126
	v_mfma_f32_32x32x16_bf16 v[50:65], v[150:153], v[70:73], v[50:65]
	v_lshlrev_b64 v[126:127], 8, v[126:127]
	v_lshl_add_u64 v[128:129], v[16:17], 0, v[126:127]
	v_lshl_add_u64 v[126:127], v[134:135], 0, v[126:127]
	global_load_dwordx4 v[130:133], v[128:129], off
	s_nop 0
	global_load_dwordx4 v[126:129], v[126:127], off
	s_waitcnt lgkmcnt(0)
	v_mfma_f32_32x32x16_bf16 v[34:49], v[224:227], v[156:159], v[34:49]
	s_waitcnt vmcnt(2)
	v_add_u32_e32 v165, s10, v187
	ds_write_b128 v165, v[118:121]
	v_add_u32_e32 v165, s10, v214
	ds_write_b128 v165, v[122:125] offset:12288
	v_exp_f32_e32 v168, v98
	v_exp_f32_e32 v169, v99
	v_mfma_f32_32x32x16_bf16 v[34:49], v[228:231], v[160:163], v[34:49]
	v_exp_f32_e32 v170, v100
	v_exp_f32_e32 v171, v101
	v_exp_f32_e32 v172, v102
	v_exp_f32_e32 v173, v103
	v_mfma_f32_32x32x16_bf16 v[34:49], v[232:235], v[66:69], v[34:49]
	v_exp_f32_e32 v174, v104
	v_exp_f32_e32 v175, v105
	v_exp_f32_e32 v176, v106
	v_exp_f32_e32 v177, v107
	v_exp_f32_e32 v178, v108
	v_mfma_f32_32x32x16_bf16 v[34:49], v[236:239], v[70:73], v[34:49]
	v_exp_f32_e32 v179, v109
	v_exp_f32_e32 v180, v110
	v_exp_f32_e32 v181, v111
	v_exp_f32_e32 v182, v112
	v_exp_f32_e32 v183, v113
	s_waitcnt lgkmcnt(0)
	s_barrier
; #define LAS __attribute__((address_space(3)))
; #define ATT_PKN(P, BASE, OUT) do { u32x4 w = {cvt_pk_bf16(P[BASE + 0], P[BASE + 1]), cvt_pk_bf16(P[BASE + 2], P[BASE + 3]), cvt_pk_bf16(P[BASE + 4], P[BASE + 5]), cvt_pk_bf16(P[BASE + 6], P[BASE + 7])}; \
;     OUT = __builtin_bit_cast(bf16x8, w); } while (0)
; __device__ __forceinline__ void finishSM(f32x16& p0, f32x16& p1, float alpha, float& l_reg, bf16x8& pa0, bf16x8& pa1, bf16x8& pa2, bf16x8& pa3) {
; #pragma unroll
;     for (int r = 0; r < 16; ++r) p1[r] = EXP_PROBE ? fmaf(p1[r], 0.001f, 1.f) : __builtin_amdgcn_exp2f(p1[r]);
;     float ps = 0.f;
; #pragma unroll
;     for (int r = 0; r < 16; ++r) ps += p0[r];
; #pragma unroll
;     for (int r = 0; r < 16; ++r) ps += p1[r];
;     { auto rr = __builtin_amdgcn_permlane32_swap(__float_as_uint(ps), __float_as_uint(ps), false, false);
;       ps = __uint_as_float(rr[0]) + __uint_as_float(rr[1]); }
;     l_reg = l_reg * alpha + ps;
;     ATT_PKN(p0, 0, pa0); ATT_PKN(p0, 8, pa1); ATT_PKN(p1, 0, pa2); ATT_PKN(p1, 8, pa3);
; }
; template <int DQK> __device__ __forceinline__ void qkt(f32x16& p0, f32x16& p1, const LAS char* buf, const bf16x8* qr, int r32, int hi, const f32x16& negm) {
; #pragma unroll
;     for (int d0 = 0; d0 < 4; ++d0) { const int ch = d0 * 2 + hi;
;         const bf16x8 b0 = *(const LAS bf16x8*)(buf + B_KN + swz64(r32, ch));
;         const bf16x8 b1 = *(const LAS bf16x8*)(buf + B_KN + swz64(32 + r32, ch));
;         p0 = __builtin_amdgcn_mfma_f32_32x32x16_bf16(b0, qr[d0], d0 == 0 ? negm : p0, 0, 0, 0);
;         p1 = __builtin_amdgcn_mfma_f32_32x32x16_bf16(b1, qr[d0], d0 == 0 ? negm : p1, 0, 0, 0); }
;     if constexpr (DQK == 96) {
; #pragma unroll
;         for (int d0 = 0; d0 < 2; ++d0) { const int ch = d0 * 2 + hi;
;             const bf16x8 b0 = *(const LAS bf16x8*)(buf + B_KR + swz32(r32, ch));
;             const bf16x8 b1 = *(const LAS bf16x8*)(buf + B_KR + swz32(32 + r32, ch));
;             p0 = __builtin_amdgcn_mfma_f32_32x32x16_bf16(b0, qr[4 + d0], p0, 0, 0, 0);
;             p1 = __builtin_amdgcn_mfma_f32_32x32x16_bf16(b1, qr[4 + d0], p1, 0, 0, 0); }
;     }
	v_add_u32_e32 v252, s10, v201
	v_add_u32_e32 v228, v252, v209
	ds_read_b128 v[224:227], v228
	ds_read_b128 v[228:231], v228 offset:4096
	v_add_u32_e32 v236, v252, v210
	ds_read_b128 v[232:235], v236
	ds_read_b128 v[236:239], v236 offset:4096
	v_add_u32_e32 v244, v252, v211
	ds_read_b128 v[240:243], v244
	ds_read_b128 v[244:247], v244 offset:4096
	v_add_u32_e32 v253, v252, v212
	ds_read_b128 v[248:251], v253
	v_exp_f32_e32 v82, v82
	v_exp_f32_e32 v83, v83
	v_exp_f32_e32 v84, v84
	v_exp_f32_e32 v85, v85
	s_waitcnt lgkmcnt(6)
	v_mfma_f32_32x32x16_bf16 v[98:113], v[224:227], v[114:117], v[18:33]
	ds_read_b128 v[224:227], v253 offset:4096
	v_exp_f32_e32 v86, v86
	v_exp_f32_e32 v87, v87
	v_exp_f32_e32 v88, v88
	v_exp_f32_e32 v89, v89
	v_cvt_pk_bf16_f32 v156, v168, v169
	v_cvt_pk_bf16_f32 v157, v170, v171
	v_add_f32_e32 v164, 0, v168
	v_add_f32_e32 v164, v169, v164
	s_waitcnt lgkmcnt(6)
	v_mfma_f32_32x32x16_bf16 v[66:81], v[228:231], v[114:117], v[18:33]
	v_exp_f32_e32 v90, v90
	v_exp_f32_e32 v91, v91
	v_exp_f32_e32 v92, v92
	v_exp_f32_e32 v93, v93
	v_cvt_pk_bf16_f32 v158, v172, v173
	v_cvt_pk_bf16_f32 v159, v174, v175
	v_add_f32_e32 v164, v170, v164
	v_add_f32_e32 v164, v171, v164
	s_waitcnt lgkmcnt(5)
	v_mfma_f32_32x32x16_bf16 v[98:113], v[232:235], v[12:15], v[98:113]
	v_exp_f32_e32 v94, v94
	v_exp_f32_e32 v95, v95
	v_exp_f32_e32 v96, v96
	v_exp_f32_e32 v97, v97
	v_cvt_pk_bf16_f32 v160, v176, v177
	v_cvt_pk_bf16_f32 v161, v178, v179
	v_add_f32_e32 v164, v172, v164
	v_add_f32_e32 v164, v173, v164
	s_waitcnt lgkmcnt(4)
	v_mfma_f32_32x32x16_bf16 v[66:81], v[236:239], v[12:15], v[66:81]
	v_cvt_pk_bf16_f32 v162, v180, v181
	v_cvt_pk_bf16_f32 v163, v182, v183
	v_add_f32_e32 v164, v174, v164
	v_add_f32_e32 v164, v175, v164
	v_add_f32_e32 v164, v176, v164
	v_add_f32_e32 v164, v177, v164
	v_add_f32_e32 v164, v178, v164
	v_add_f32_e32 v164, v179, v164
	v_add_f32_e32 v164, v180, v164
	v_add_f32_e32 v164, v181, v164
	v_add_f32_e32 v164, v182, v164
	v_add_f32_e32 v164, v183, v164
	s_waitcnt lgkmcnt(3)
	v_mfma_f32_32x32x16_bf16 v[98:113], v[240:243], v[8:11], v[98:113]
	v_add_u32_e32 v253, s1, v213
	ds_read_b64_tr_b16 v[168:169], v253 offset:0
	ds_read_b64_tr_b16 v[170:171], v253 offset:1024
	ds_read_b64_tr_b16 v[172:173], v253 offset:2048
	ds_read_b64_tr_b16 v[174:175], v253 offset:3072
	v_add_f32_e32 v164, v82, v164
	v_add_f32_e32 v164, v83, v164
	v_add_f32_e32 v164, v84, v164
	v_add_f32_e32 v164, v85, v164
	s_waitcnt lgkmcnt(6)
	v_mfma_f32_32x32x16_bf16 v[66:81], v[244:247], v[8:11], v[66:81]
	ds_read_b64_tr_b16 v[176:177], v253 offset:4096
	ds_read_b64_tr_b16 v[178:179], v253 offset:5120
	ds_read_b64_tr_b16 v[180:181], v253 offset:6144
	ds_read_b64_tr_b16 v[182:183], v253 offset:7168
	v_add_f32_e32 v164, v86, v164
	v_add_f32_e32 v164, v87, v164
	v_add_f32_e32 v164, v88, v164
	v_add_f32_e32 v164, v89, v164
	s_waitcnt lgkmcnt(9)
	v_mfma_f32_32x32x16_bf16 v[98:113], v[248:251], v[4:7], v[98:113]
	v_add_f32_e32 v164, v90, v164
	v_add_f32_e32 v164, v91, v164
	v_add_f32_e32 v164, v92, v164
	v_add_f32_e32 v164, v93, v164
	s_waitcnt lgkmcnt(8)
	v_mfma_f32_32x32x16_bf16 v[66:81], v[224:227], v[4:7], v[66:81]
	ds_read_b64_tr_b16 v[224:225], v253 offset:512
	ds_read_b64_tr_b16 v[226:227], v253 offset:1536
	ds_read_b64_tr_b16 v[228:229], v253 offset:2560
	ds_read_b64_tr_b16 v[230:231], v253 offset:3584
	ds_read_b64_tr_b16 v[232:233], v253 offset:4608
	ds_read_b64_tr_b16 v[234:235], v253 offset:5632
	ds_read_b64_tr_b16 v[236:237], v253 offset:6656
	ds_read_b64_tr_b16 v[238:239], v253 offset:7680
	s_waitcnt lgkmcnt(8)
	v_mfma_f32_32x32x16_bf16 v[50:65], v[168:171], v[156:159], v[50:65]
	v_add_f32_e32 v164, v94, v164
	v_add_f32_e32 v164, v95, v164
	v_add_f32_e32 v164, v96, v164
	v_add_f32_e32 v164, v97, v164
	v_mov_b32_e32 v165, v164
	v_mfma_f32_32x32x16_bf16 v[50:65], v[172:175], v[160:163], v[50:65]
	v_cvt_pk_bf16_f32 v82, v82, v83
	v_cvt_pk_bf16_f32 v83, v84, v85
	v_cvt_pk_bf16_f32 v84, v86, v87
	v_cvt_pk_bf16_f32 v85, v88, v89
	v_cvt_pk_bf16_f32 v86, v90, v91
	v_cvt_pk_bf16_f32 v87, v92, v93
	v_cvt_pk_bf16_f32 v88, v94, v95
	v_cvt_pk_bf16_f32 v89, v96, v97
	v_permlane32_swap_b32_e32 v164, v165
	v_mfma_f32_32x32x16_bf16 v[50:65], v[176:179], v[82:85], v[50:65]
	v_mfma_f32_32x32x16_bf16 v[50:65], v[180:183], v[86:89], v[50:65]
	s_cmp_ge_u32 s13, s30
	s_cbranch_scc1 .Lgqa_b_noload
	s_cmp_lt_u32 s13, s31
	s_cselect_b32 s9, 0, s31
	s_cselect_b32 s35, s12, s29
	s_lshl_b32 s9, s9, 6
	s_sub_i32 s9, s35, s9
	v_add_u32_e32 v118, s9, v137
	v_ashrrev_i32_e32 v119, 31, v118
	v_lshlrev_b64 v[118:119], 8, v[118:119]
	v_lshl_add_u64 v[120:121], v[16:17], 0, v[118:119]
	v_lshl_add_u64 v[122:123], v[134:135], 0, v[118:119]
	global_load_dwordx4 v[118:121], v[120:121], off
	s_nop 0
	global_load_dwordx4 v[122:125], v[122:123], off
